# dead wait-state trimming: the 4x s_nop 15 behind each fp8 GEMM unit's K-loop reduced to one (16 states already exceed the MFMA result latency); on top of the MLA nop fill
# speedup vs baseline: 1.0007x; 1.0007x over previous
.LBB0_1607:
	ds_read_b128 v[24:27], v167
	ds_read_b128 v[28:31], v167 offset:1024
	ds_read_b128 v[196:199], v167 offset:2048
	ds_read_b128 v[200:203], v167 offset:3072
	ds_read_b128 v[12:15], v173
	ds_read_b128 v[16:19], v173 offset:1024
	ds_read_b128 v[4:7], v173 offset:2048
	ds_read_b128 v[8:11], v173 offset:3072
	s_cmp_eq_u32 s45, 4
	s_cselect_b64 vcc, -1, 0
	s_and_b64 s[46:47], vcc, exec
	s_cselect_b32 s47, s0, s48
	s_cselect_b32 s56, 0, s50
	s_cselect_b32 s46, s1, s49
	s_cselect_b32 s57, 0, s51
	s_add_u32 s54, s47, s56
	v_cndmask_b32_e32 v20, v174, v192, vcc
	s_addc_u32 s55, s46, s57
	v_cndmask_b32_e32 v32, v172, v191, vcc
	v_cndmask_b32_e32 v178, v170, v189, vcc
	v_cndmask_b32_e32 v179, v168, v190, vcc
	s_mov_b32 m0, s3
	v_lshl_add_u64 v[22:23], s[52:53], 0, v[170:171]
	ds_read_b128 v[204:207], v175
	ds_read_b128 v[208:211], v175 offset:1024
	ds_read_b128 v[216:219], v175 offset:2048
	ds_read_b128 v[220:223], v175 offset:3072
	ds_read_b128 v[224:227], v175 offset:4096
	ds_read_b128 v[228:231], v175 offset:5120
	ds_read_b128 v[232:235], v175 offset:6144
	ds_read_b128 v[236:239], v175 offset:7168
	global_load_lds_dwordx4 v[22:23], off
	v_lshl_add_u64 v[22:23], s[52:53], 0, v[168:169]
	s_mov_b32 m0, s13
	s_nop 0
	global_load_lds_dwordx4 v[22:23], off
	s_waitcnt vmcnt(8)
	s_waitcnt lgkmcnt(0)
	s_barrier
	s_setprio 1
	s_waitcnt lgkmcnt(0)
	v_mfma_scale_f32_16x16x128_f8f6f4 v[156:159], v[24:31], v[204:211], v[156:159], v243, v243 op_sel_hi:[0,0,0]
	v_mfma_scale_f32_16x16x128_f8f6f4 v[160:163], v[196:203], v[204:211], v[160:163], v243, v243 op_sel_hi:[0,0,0]
	v_mfma_scale_f32_16x16x128_f8f6f4 v[140:143], v[24:31], v[216:223], v[140:143], v243, v243 op_sel_hi:[0,0,0]
	v_mfma_scale_f32_16x16x128_f8f6f4 v[144:147], v[196:203], v[216:223], v[144:147], v243, v243 op_sel_hi:[0,0,0]
	v_mfma_scale_f32_16x16x128_f8f6f4 v[124:127], v[24:31], v[224:231], v[124:127], v243, v243 op_sel_hi:[0,0,0]
	v_mfma_scale_f32_16x16x128_f8f6f4 v[128:131], v[196:203], v[224:231], v[128:131], v243, v243 op_sel_hi:[0,0,0]
	v_mfma_scale_f32_16x16x128_f8f6f4 v[108:111], v[24:31], v[232:239], v[108:111], v243, v243 op_sel_hi:[0,0,0]
	v_mfma_scale_f32_16x16x128_f8f6f4 v[112:115], v[196:203], v[232:239], v[112:115], v243, v243 op_sel_hi:[0,0,0]
	s_setprio 0
	s_setprio 1
	v_mfma_scale_f32_16x16x128_f8f6f4 v[148:151], v[12:19], v[204:211], v[148:151], v243, v243 op_sel_hi:[0,0,0]
	v_mfma_scale_f32_16x16x128_f8f6f4 v[152:155], v[4:11], v[204:211], v[152:155], v243, v243 op_sel_hi:[0,0,0]
	v_mfma_scale_f32_16x16x128_f8f6f4 v[132:135], v[12:19], v[216:223], v[132:135], v243, v243 op_sel_hi:[0,0,0]
	v_mfma_scale_f32_16x16x128_f8f6f4 v[136:139], v[4:11], v[216:223], v[136:139], v243, v243 op_sel_hi:[0,0,0]
	v_mfma_scale_f32_16x16x128_f8f6f4 v[116:119], v[12:19], v[224:231], v[116:119], v243, v243 op_sel_hi:[0,0,0]
	v_mfma_scale_f32_16x16x128_f8f6f4 v[120:123], v[4:11], v[224:231], v[120:123], v243, v243 op_sel_hi:[0,0,0]
	v_mfma_scale_f32_16x16x128_f8f6f4 v[100:103], v[12:19], v[232:239], v[100:103], v243, v243 op_sel_hi:[0,0,0]
	v_mfma_scale_f32_16x16x128_f8f6f4 v[104:107], v[4:11], v[232:239], v[104:107], v243, v243 op_sel_hi:[0,0,0]
	s_setprio 0
	s_barrier
	s_mov_b32 m0, s26
	ds_read_b128 v[204:207], v175 offset:16384
	ds_read_b128 v[208:211], v175 offset:17408
	ds_read_b128 v[216:219], v175 offset:18432
	ds_read_b128 v[220:223], v175 offset:19456
	ds_read_b128 v[224:227], v175 offset:20480
	ds_read_b128 v[228:231], v175 offset:21504
	ds_read_b128 v[232:235], v175 offset:22528
	ds_read_b128 v[236:239], v175 offset:23552
	global_load_lds_dwordx4 v2, s[54:55]
	s_mov_b32 m0, s27
	s_add_u32 s46, s54, 0x20000
	global_load_lds_dwordx4 v164, s[54:55]
	s_addc_u32 s47, s55, 0
	s_mov_b32 m0, s28
	s_add_u32 s56, s14, s56
	global_load_lds_dwordx4 v2, s[46:47]
	s_mov_b32 m0, s33
	s_addc_u32 s57, s15, s57
	global_load_lds_dwordx4 v164, s[46:47]
	s_mov_b32 m0, s67
	v_mov_b32_e32 v165, v3
	global_load_lds_dwordx4 v20, s[56:57]
	s_mov_b32 m0, s68
	v_mov_b32_e32 v21, v3
	global_load_lds_dwordx4 v32, s[56:57]
	s_waitcnt vmcnt(8)
	s_waitcnt lgkmcnt(0)
	v_mov_b32_e32 v33, v3
	v_lshl_add_u64 v[34:35], s[54:55], 0, v[2:3]
	v_lshl_add_u64 v[176:177], s[54:55], 0, v[164:165]
	v_lshl_add_u64 v[22:23], s[56:57], 0, v[20:21]
	v_lshl_add_u64 v[20:21], s[56:57], 0, v[32:33]
	s_barrier
	s_setprio 1
	s_waitcnt lgkmcnt(0)
	v_mfma_scale_f32_16x16x128_f8f6f4 v[92:95], v[24:31], v[204:211], v[92:95], v243, v243 op_sel_hi:[0,0,0]
	v_mfma_scale_f32_16x16x128_f8f6f4 v[96:99], v[196:203], v[204:211], v[96:99], v243, v243 op_sel_hi:[0,0,0]
	v_mfma_scale_f32_16x16x128_f8f6f4 v[76:79], v[24:31], v[216:223], v[76:79], v243, v243 op_sel_hi:[0,0,0]
	v_mfma_scale_f32_16x16x128_f8f6f4 v[80:83], v[196:203], v[216:223], v[80:83], v243, v243 op_sel_hi:[0,0,0]
	v_mfma_scale_f32_16x16x128_f8f6f4 v[60:63], v[24:31], v[224:231], v[60:63], v243, v243 op_sel_hi:[0,0,0]
	v_mfma_scale_f32_16x16x128_f8f6f4 v[64:67], v[196:203], v[224:231], v[64:67], v243, v243 op_sel_hi:[0,0,0]
	v_mfma_scale_f32_16x16x128_f8f6f4 v[40:43], v[24:31], v[232:239], v[40:43], v243, v243 op_sel_hi:[0,0,0]
	v_mfma_scale_f32_16x16x128_f8f6f4 v[44:47], v[196:203], v[232:239], v[44:47], v243, v243 op_sel_hi:[0,0,0]
	s_setprio 0
	s_setprio 1
	v_mfma_scale_f32_16x16x128_f8f6f4 v[84:87], v[12:19], v[204:211], v[84:87], v243, v243 op_sel_hi:[0,0,0]
	v_mfma_scale_f32_16x16x128_f8f6f4 v[88:91], v[4:11], v[204:211], v[88:91], v243, v243 op_sel_hi:[0,0,0]
	v_mfma_scale_f32_16x16x128_f8f6f4 v[68:71], v[12:19], v[216:223], v[68:71], v243, v243 op_sel_hi:[0,0,0]
	v_mfma_scale_f32_16x16x128_f8f6f4 v[72:75], v[4:11], v[216:223], v[72:75], v243, v243 op_sel_hi:[0,0,0]
	v_mfma_scale_f32_16x16x128_f8f6f4 v[52:55], v[12:19], v[224:231], v[52:55], v243, v243 op_sel_hi:[0,0,0]
	v_mfma_scale_f32_16x16x128_f8f6f4 v[56:59], v[4:11], v[224:231], v[56:59], v243, v243 op_sel_hi:[0,0,0]
	v_mfma_scale_f32_16x16x128_f8f6f4 v[36:39], v[12:19], v[232:239], v[36:39], v243, v243 op_sel_hi:[0,0,0]
	v_mfma_scale_f32_16x16x128_f8f6f4 v[48:51], v[4:11], v[232:239], v[48:51], v243, v243 op_sel_hi:[0,0,0]
	s_setprio 0
	s_barrier
; #define PG8_BAR __builtin_amdgcn_s_barrier()
; template <class P, bool ALIGN_EPI>
; __device__ __forceinline__ void gemm_phase(ldsp lds, ldsp tab, const P& S) {
;     ...
;             for (int t = 2; t < nt; t += 2) PG8_TRIP(t, PG8_MMA);
;         } else {
;             for (int t = 0; t < nt; t += 2) PG8_TRIP(t, PG8_MMA);
;         }
;         if constexpr (P::FP8) asm volatile("s_nop 15\n\ts_nop 15\n\ts_nop 15\n\ts_nop 15" ::: "memory");
;         if constexpr (ALIGN_EPI) { if (wr == 0) PG8_BAR; }
	ds_read_b128 v[24:27], v193
	ds_read_b128 v[28:31], v193 offset:1024
	ds_read_b128 v[196:199], v193 offset:2048
	ds_read_b128 v[200:203], v193 offset:3072
	ds_read_b128 v[12:15], v194
	ds_read_b128 v[16:19], v194 offset:1024
	ds_read_b128 v[4:7], v194 offset:2048
	ds_read_b128 v[8:11], v194 offset:3072
	s_mov_b32 m0, s69
	ds_read_b128 v[204:207], v175 offset:32768
	ds_read_b128 v[208:211], v175 offset:33792
	ds_read_b128 v[216:219], v175 offset:34816
	ds_read_b128 v[220:223], v175 offset:35840
	ds_read_b128 v[224:227], v175 offset:36864
	ds_read_b128 v[228:231], v175 offset:37888
	ds_read_b128 v[232:235], v175 offset:38912
	ds_read_b128 v[236:239], v175 offset:39936
	global_load_lds_dwordx4 v178, s[56:57]
	s_mov_b32 m0, s70
	s_nop 0
	global_load_lds_dwordx4 v179, s[56:57]
	s_waitcnt vmcnt(8)
	s_waitcnt lgkmcnt(0)
	s_barrier
	s_setprio 1
	s_waitcnt lgkmcnt(0)
	v_mfma_scale_f32_16x16x128_f8f6f4 v[156:159], v[24:31], v[204:211], v[156:159], v243, v243 op_sel_hi:[0,0,0]
	v_mfma_scale_f32_16x16x128_f8f6f4 v[160:163], v[196:203], v[204:211], v[160:163], v243, v243 op_sel_hi:[0,0,0]
	v_mfma_scale_f32_16x16x128_f8f6f4 v[140:143], v[24:31], v[216:223], v[140:143], v243, v243 op_sel_hi:[0,0,0]
	v_mfma_scale_f32_16x16x128_f8f6f4 v[144:147], v[196:203], v[216:223], v[144:147], v243, v243 op_sel_hi:[0,0,0]
	v_mfma_scale_f32_16x16x128_f8f6f4 v[124:127], v[24:31], v[224:231], v[124:127], v243, v243 op_sel_hi:[0,0,0]
	v_mfma_scale_f32_16x16x128_f8f6f4 v[128:131], v[196:203], v[224:231], v[128:131], v243, v243 op_sel_hi:[0,0,0]
	v_mfma_scale_f32_16x16x128_f8f6f4 v[108:111], v[24:31], v[232:239], v[108:111], v243, v243 op_sel_hi:[0,0,0]
	v_mfma_scale_f32_16x16x128_f8f6f4 v[112:115], v[196:203], v[232:239], v[112:115], v243, v243 op_sel_hi:[0,0,0]
	s_setprio 0
	s_setprio 1
	v_mfma_scale_f32_16x16x128_f8f6f4 v[148:151], v[12:19], v[204:211], v[148:151], v243, v243 op_sel_hi:[0,0,0]
	v_mfma_scale_f32_16x16x128_f8f6f4 v[152:155], v[4:11], v[204:211], v[152:155], v243, v243 op_sel_hi:[0,0,0]
	v_mfma_scale_f32_16x16x128_f8f6f4 v[132:135], v[12:19], v[216:223], v[132:135], v243, v243 op_sel_hi:[0,0,0]
	v_mfma_scale_f32_16x16x128_f8f6f4 v[136:139], v[4:11], v[216:223], v[136:139], v243, v243 op_sel_hi:[0,0,0]
	v_mfma_scale_f32_16x16x128_f8f6f4 v[116:119], v[12:19], v[224:231], v[116:119], v243, v243 op_sel_hi:[0,0,0]
	v_mfma_scale_f32_16x16x128_f8f6f4 v[120:123], v[4:11], v[224:231], v[120:123], v243, v243 op_sel_hi:[0,0,0]
	v_mfma_scale_f32_16x16x128_f8f6f4 v[100:103], v[12:19], v[232:239], v[100:103], v243, v243 op_sel_hi:[0,0,0]
	v_mfma_scale_f32_16x16x128_f8f6f4 v[104:107], v[4:11], v[232:239], v[104:107], v243, v243 op_sel_hi:[0,0,0]
	s_setprio 0
	s_barrier
	s_mov_b32 m0, s34
	v_lshl_add_u64 v[32:33], v[34:35], 0, s[24:25]
	ds_read_b128 v[204:207], v175 offset:49152
	ds_read_b128 v[208:211], v175 offset:50176
	ds_read_b128 v[216:219], v175 offset:51200
	ds_read_b128 v[220:223], v175 offset:52224
	ds_read_b128 v[224:227], v175 offset:53248
	ds_read_b128 v[228:231], v175 offset:54272
	ds_read_b128 v[232:235], v175 offset:55296
	ds_read_b128 v[236:239], v175 offset:56320
	global_load_lds_dwordx4 v[32:33], off
	v_lshl_add_u64 v[32:33], v[176:177], 0, s[24:25]
	s_mov_b32 m0, s35
	s_add_u32 s46, s54, 0x20080
	global_load_lds_dwordx4 v[32:33], off
	s_addc_u32 s47, s55, 0
	s_mov_b32 m0, s41
	v_lshl_add_u64 v[22:23], v[22:23], 0, s[24:25]
	global_load_lds_dwordx4 v2, s[46:47]
	s_mov_b32 m0, s43
	v_lshl_add_u64 v[20:21], v[20:21], 0, s[24:25]
	global_load_lds_dwordx4 v164, s[46:47]
	s_mov_b32 m0, s72
	s_nop 0
	global_load_lds_dwordx4 v[22:23], off
	s_mov_b32 m0, s73
	s_nop 0
	global_load_lds_dwordx4 v[20:21], off
	s_waitcnt vmcnt(8)
	s_waitcnt lgkmcnt(0)
	s_barrier
	s_setprio 1
	s_waitcnt lgkmcnt(0)
	v_mfma_scale_f32_16x16x128_f8f6f4 v[92:95], v[24:31], v[204:211], v[92:95], v243, v243 op_sel_hi:[0,0,0]
	v_mfma_scale_f32_16x16x128_f8f6f4 v[96:99], v[196:203], v[204:211], v[96:99], v243, v243 op_sel_hi:[0,0,0]
	v_mfma_scale_f32_16x16x128_f8f6f4 v[76:79], v[24:31], v[216:223], v[76:79], v243, v243 op_sel_hi:[0,0,0]
	v_mfma_scale_f32_16x16x128_f8f6f4 v[80:83], v[196:203], v[216:223], v[80:83], v243, v243 op_sel_hi:[0,0,0]
	v_mfma_scale_f32_16x16x128_f8f6f4 v[60:63], v[24:31], v[224:231], v[60:63], v243, v243 op_sel_hi:[0,0,0]
	v_mfma_scale_f32_16x16x128_f8f6f4 v[64:67], v[196:203], v[224:231], v[64:67], v243, v243 op_sel_hi:[0,0,0]
	v_mfma_scale_f32_16x16x128_f8f6f4 v[40:43], v[24:31], v[232:239], v[40:43], v243, v243 op_sel_hi:[0,0,0]
	v_mfma_scale_f32_16x16x128_f8f6f4 v[44:47], v[196:203], v[232:239], v[44:47], v243, v243 op_sel_hi:[0,0,0]
	s_setprio 0
	s_setprio 1
	v_mfma_scale_f32_16x16x128_f8f6f4 v[84:87], v[12:19], v[204:211], v[84:87], v243, v243 op_sel_hi:[0,0,0]
	v_mfma_scale_f32_16x16x128_f8f6f4 v[88:91], v[4:11], v[204:211], v[88:91], v243, v243 op_sel_hi:[0,0,0]
	v_mfma_scale_f32_16x16x128_f8f6f4 v[68:71], v[12:19], v[216:223], v[68:71], v243, v243 op_sel_hi:[0,0,0]
	v_mfma_scale_f32_16x16x128_f8f6f4 v[72:75], v[4:11], v[216:223], v[72:75], v243, v243 op_sel_hi:[0,0,0]
	v_mfma_scale_f32_16x16x128_f8f6f4 v[52:55], v[12:19], v[224:231], v[52:55], v243, v243 op_sel_hi:[0,0,0]
	v_mfma_scale_f32_16x16x128_f8f6f4 v[56:59], v[4:11], v[224:231], v[56:59], v243, v243 op_sel_hi:[0,0,0]
	v_mfma_scale_f32_16x16x128_f8f6f4 v[36:39], v[12:19], v[232:239], v[36:39], v243, v243 op_sel_hi:[0,0,0]
	v_mfma_scale_f32_16x16x128_f8f6f4 v[48:51], v[4:11], v[232:239], v[48:51], v243, v243 op_sel_hi:[0,0,0]
	s_setprio 0
	s_barrier
	s_add_i32 s45, s45, 2
	s_add_u32 s50, s50, 0x100
	s_addc_u32 s51, s51, 0
	s_add_u32 s52, s52, 0x100
	s_addc_u32 s53, s53, 0
	s_cmp_gt_u32 s45, 5
	s_cbranch_scc0 .LBB0_1607
	s_nop 15
	s_and_b64 vcc, exec, s[20:21]
	s_cbranch_vccz .LBB0_1610
	s_barrier

.LBB0_1718:
	s_add_u32 s22, s20, 0xfff90080
	s_addc_u32 s23, s21, -1
	s_cmp_eq_u32 s63, 24
	s_cselect_b64 vcc, -1, 0
	v_cndmask_b32_e32 v5, v171, v175, vcc
	v_cndmask_b32_e32 v4, v170, v174, vcc
	s_cselect_b32 s23, 0, s23
	s_cselect_b32 s22, 0, s22
	v_lshl_add_u64 v[176:177], v[4:5], 0, s[22:23]
	ds_read_b128 v[28:31], v173
	ds_read_b128 v[32:35], v173 offset:1024
	ds_read_b128 v[20:23], v173 offset:2048
	ds_read_b128 v[24:27], v173 offset:3072
	ds_read_b128 v[12:15], v187
	ds_read_b128 v[16:19], v187 offset:1024
	ds_read_b128 v[4:7], v187 offset:2048
	ds_read_b128 v[8:11], v187 offset:3072
	s_cselect_b32 s64, s0, s16
	s_cselect_b32 s65, s1, s17
	s_add_u32 s66, s16, s20
	s_mov_b32 m0, s3
	s_addc_u32 s67, s17, s21
	ds_read_b128 v[190:193], v186
	ds_read_b128 v[194:197], v186 offset:1024
	ds_read_b128 v[198:201], v186 offset:2048
	ds_read_b128 v[202:205], v186 offset:3072
	ds_read_b128 v[216:219], v186 offset:4096
	ds_read_b128 v[220:223], v186 offset:5120
	ds_read_b128 v[224:227], v186 offset:6144
	ds_read_b128 v[228:231], v186 offset:7168
	global_load_lds_dwordx4 v2, s[66:67]
	s_mov_b32 m0, s19
	v_mov_b32_e32 v167, v3
	global_load_lds_dwordx4 v166, s[66:67]
	s_waitcnt vmcnt(8)
	s_waitcnt lgkmcnt(0)
	s_barrier
	s_setprio 1
	s_waitcnt lgkmcnt(0)
	v_mfma_scale_f32_16x16x128_f8f6f4 v[148:151], v[28:35], v[190:197], v[148:151], v243, v243 op_sel_hi:[0,0,0]
	v_mfma_scale_f32_16x16x128_f8f6f4 v[152:155], v[20:27], v[190:197], v[152:155], v243, v243 op_sel_hi:[0,0,0]
	v_mfma_scale_f32_16x16x128_f8f6f4 v[136:139], v[28:35], v[198:205], v[136:139], v243, v243 op_sel_hi:[0,0,0]
	v_mfma_scale_f32_16x16x128_f8f6f4 v[132:135], v[20:27], v[198:205], v[132:135], v243, v243 op_sel_hi:[0,0,0]
	v_mfma_scale_f32_16x16x128_f8f6f4 v[120:123], v[28:35], v[216:223], v[120:123], v243, v243 op_sel_hi:[0,0,0]
	v_mfma_scale_f32_16x16x128_f8f6f4 v[116:119], v[20:27], v[216:223], v[116:119], v243, v243 op_sel_hi:[0,0,0]
	v_mfma_scale_f32_16x16x128_f8f6f4 v[92:95], v[28:35], v[224:231], v[92:95], v243, v243 op_sel_hi:[0,0,0]
	v_mfma_scale_f32_16x16x128_f8f6f4 v[84:87], v[20:27], v[224:231], v[84:87], v243, v243 op_sel_hi:[0,0,0]
	s_setprio 0
	s_setprio 1
	v_mfma_scale_f32_16x16x128_f8f6f4 v[156:159], v[12:19], v[190:197], v[156:159], v243, v243 op_sel_hi:[0,0,0]
	v_mfma_scale_f32_16x16x128_f8f6f4 v[160:163], v[4:11], v[190:197], v[160:163], v243, v243 op_sel_hi:[0,0,0]
	v_mfma_scale_f32_16x16x128_f8f6f4 v[144:147], v[12:19], v[198:205], v[144:147], v243, v243 op_sel_hi:[0,0,0]
	v_mfma_scale_f32_16x16x128_f8f6f4 v[140:143], v[4:11], v[198:205], v[140:143], v243, v243 op_sel_hi:[0,0,0]
	v_mfma_scale_f32_16x16x128_f8f6f4 v[128:131], v[12:19], v[216:223], v[128:131], v243, v243 op_sel_hi:[0,0,0]
	v_mfma_scale_f32_16x16x128_f8f6f4 v[124:127], v[4:11], v[216:223], v[124:127], v243, v243 op_sel_hi:[0,0,0]
	v_mfma_scale_f32_16x16x128_f8f6f4 v[96:99], v[12:19], v[224:231], v[96:99], v243, v243 op_sel_hi:[0,0,0]
	v_mfma_scale_f32_16x16x128_f8f6f4 v[88:91], v[4:11], v[224:231], v[88:91], v243, v243 op_sel_hi:[0,0,0]
	s_setprio 0
	s_barrier
	s_mov_b32 m0, s26
	v_readfirstlane_b32 s66, v176
	v_readfirstlane_b32 s67, v177
	ds_read_b128 v[190:193], v186 offset:16384
	ds_read_b128 v[194:197], v186 offset:17408
	ds_read_b128 v[198:201], v186 offset:18432
	ds_read_b128 v[202:205], v186 offset:19456
	ds_read_b128 v[216:219], v186 offset:20480
	ds_read_b128 v[220:223], v186 offset:21504
	ds_read_b128 v[224:227], v186 offset:22528
	ds_read_b128 v[228:231], v186 offset:23552
	global_load_lds_dwordx4 v164, s[66:67]
	s_mov_b32 m0, s27
	v_lshl_add_u64 v[178:179], v[176:177], 0, s[86:87]
	global_load_lds_dwordx4 v168, s[66:67]
	v_readfirstlane_b32 s66, v178
	v_readfirstlane_b32 s67, v179
	s_mov_b32 m0, s28
	s_add_u32 s22, s64, s22
	s_addc_u32 s23, s65, s23
	v_mov_b32_e32 v165, v3
	v_mov_b32_e32 v169, v3
	global_load_lds_dwordx4 v164, s[66:67]
	s_mov_b32 m0, s33
	v_lshl_add_u64 v[182:183], v[176:177], 0, v[164:165]
	global_load_lds_dwordx4 v168, s[66:67]
	s_mov_b32 m0, s44
	v_lshl_add_u64 v[206:207], v[176:177], 0, v[168:169]
	global_load_lds_dwordx4 v2, s[22:23]
	s_mov_b32 m0, s45
	v_lshl_add_u64 v[180:181], s[22:23], 0, v[2:3]
	global_load_lds_dwordx4 v166, s[22:23]
	s_waitcnt vmcnt(8)
	s_waitcnt lgkmcnt(0)
	v_lshl_add_u64 v[178:179], s[22:23], 0, v[166:167]
	s_barrier
	s_setprio 1
	s_waitcnt lgkmcnt(0)
	v_mfma_scale_f32_16x16x128_f8f6f4 v[104:107], v[28:35], v[190:197], v[104:107], v243, v243 op_sel_hi:[0,0,0]
	v_mfma_scale_f32_16x16x128_f8f6f4 v[100:103], v[20:27], v[190:197], v[100:103], v243, v243 op_sel_hi:[0,0,0]
	v_mfma_scale_f32_16x16x128_f8f6f4 v[76:79], v[28:35], v[198:205], v[76:79], v243, v243 op_sel_hi:[0,0,0]
	v_mfma_scale_f32_16x16x128_f8f6f4 v[68:71], v[20:27], v[198:205], v[68:71], v243, v243 op_sel_hi:[0,0,0]
	v_mfma_scale_f32_16x16x128_f8f6f4 v[64:67], v[28:35], v[216:223], v[64:67], v243, v243 op_sel_hi:[0,0,0]
	v_mfma_scale_f32_16x16x128_f8f6f4 v[60:63], v[20:27], v[216:223], v[60:63], v243, v243 op_sel_hi:[0,0,0]
	v_mfma_scale_f32_16x16x128_f8f6f4 v[48:51], v[28:35], v[224:231], v[48:51], v243, v243 op_sel_hi:[0,0,0]
	v_mfma_scale_f32_16x16x128_f8f6f4 v[44:47], v[20:27], v[224:231], v[44:47], v243, v243 op_sel_hi:[0,0,0]
	s_setprio 0
	s_setprio 1
	v_mfma_scale_f32_16x16x128_f8f6f4 v[112:115], v[12:19], v[190:197], v[112:115], v243, v243 op_sel_hi:[0,0,0]
	v_mfma_scale_f32_16x16x128_f8f6f4 v[108:111], v[4:11], v[190:197], v[108:111], v243, v243 op_sel_hi:[0,0,0]
	v_mfma_scale_f32_16x16x128_f8f6f4 v[80:83], v[12:19], v[198:205], v[80:83], v243, v243 op_sel_hi:[0,0,0]
	v_mfma_scale_f32_16x16x128_f8f6f4 v[72:75], v[4:11], v[198:205], v[72:75], v243, v243 op_sel_hi:[0,0,0]
	v_mfma_scale_f32_16x16x128_f8f6f4 v[56:59], v[12:19], v[216:223], v[56:59], v243, v243 op_sel_hi:[0,0,0]
	v_mfma_scale_f32_16x16x128_f8f6f4 v[52:55], v[4:11], v[216:223], v[52:55], v243, v243 op_sel_hi:[0,0,0]
	v_mfma_scale_f32_16x16x128_f8f6f4 v[40:43], v[12:19], v[224:231], v[40:43], v243, v243 op_sel_hi:[0,0,0]
	v_mfma_scale_f32_16x16x128_f8f6f4 v[36:39], v[4:11], v[224:231], v[36:39], v243, v243 op_sel_hi:[0,0,0]
	s_setprio 0
	s_barrier
; #define PG8_BAR __builtin_amdgcn_s_barrier()
; template <class P, bool ALIGN_EPI>
; __device__ __forceinline__ void gemm_phase(ldsp lds, ldsp tab, const P& S) {
;     ...
;             for (int t = 2; t < nt; t += 2) PG8_TRIP(t, PG8_MMA);
;         } else {
;             for (int t = 0; t < nt; t += 2) PG8_TRIP(t, PG8_MMA);
;         }
;         if constexpr (P::FP8) asm volatile("s_nop 15\n\ts_nop 15\n\ts_nop 15\n\ts_nop 15" ::: "memory");
;         if constexpr (ALIGN_EPI) { if (wr == 0) PG8_BAR; }
	ds_read_b128 v[20:23], v188
	ds_read_b128 v[24:27], v188 offset:1024
	ds_read_b128 v[28:31], v188 offset:2048
	ds_read_b128 v[32:35], v188 offset:3072
	ds_read_b128 v[12:15], v189
	ds_read_b128 v[16:19], v189 offset:1024
	ds_read_b128 v[4:7], v189 offset:2048
	ds_read_b128 v[8:11], v189 offset:3072
	s_add_u32 s22, s22, 0x70000
	s_addc_u32 s23, s23, 0
	s_mov_b32 m0, s48
	ds_read_b128 v[190:193], v186 offset:32768
	ds_read_b128 v[194:197], v186 offset:33792
	ds_read_b128 v[198:201], v186 offset:34816
	ds_read_b128 v[202:205], v186 offset:35840
	ds_read_b128 v[216:219], v186 offset:36864
	ds_read_b128 v[220:223], v186 offset:37888
	ds_read_b128 v[224:227], v186 offset:38912
	ds_read_b128 v[228:231], v186 offset:39936
	global_load_lds_dwordx4 v2, s[22:23]
	s_mov_b32 m0, s49
	s_nop 0
	global_load_lds_dwordx4 v166, s[22:23]
	s_waitcnt vmcnt(8)
	s_waitcnt lgkmcnt(0)
	s_barrier
	s_setprio 1
	s_waitcnt lgkmcnt(0)
	v_mfma_scale_f32_16x16x128_f8f6f4 v[148:151], v[20:27], v[190:197], v[148:151], v243, v243 op_sel_hi:[0,0,0]
	v_mfma_scale_f32_16x16x128_f8f6f4 v[152:155], v[28:35], v[190:197], v[152:155], v243, v243 op_sel_hi:[0,0,0]
	v_mfma_scale_f32_16x16x128_f8f6f4 v[136:139], v[20:27], v[198:205], v[136:139], v243, v243 op_sel_hi:[0,0,0]
	v_mfma_scale_f32_16x16x128_f8f6f4 v[132:135], v[28:35], v[198:205], v[132:135], v243, v243 op_sel_hi:[0,0,0]
	v_mfma_scale_f32_16x16x128_f8f6f4 v[120:123], v[20:27], v[216:223], v[120:123], v243, v243 op_sel_hi:[0,0,0]
	v_mfma_scale_f32_16x16x128_f8f6f4 v[116:119], v[28:35], v[216:223], v[116:119], v243, v243 op_sel_hi:[0,0,0]
	v_mfma_scale_f32_16x16x128_f8f6f4 v[92:95], v[20:27], v[224:231], v[92:95], v243, v243 op_sel_hi:[0,0,0]
	v_mfma_scale_f32_16x16x128_f8f6f4 v[84:87], v[28:35], v[224:231], v[84:87], v243, v243 op_sel_hi:[0,0,0]
	s_setprio 0
	s_setprio 1
	v_mfma_scale_f32_16x16x128_f8f6f4 v[156:159], v[12:19], v[190:197], v[156:159], v243, v243 op_sel_hi:[0,0,0]
	v_mfma_scale_f32_16x16x128_f8f6f4 v[160:163], v[4:11], v[190:197], v[160:163], v243, v243 op_sel_hi:[0,0,0]
	v_mfma_scale_f32_16x16x128_f8f6f4 v[144:147], v[12:19], v[198:205], v[144:147], v243, v243 op_sel_hi:[0,0,0]
	v_mfma_scale_f32_16x16x128_f8f6f4 v[140:143], v[4:11], v[198:205], v[140:143], v243, v243 op_sel_hi:[0,0,0]
	v_mfma_scale_f32_16x16x128_f8f6f4 v[128:131], v[12:19], v[216:223], v[128:131], v243, v243 op_sel_hi:[0,0,0]
	v_mfma_scale_f32_16x16x128_f8f6f4 v[124:127], v[4:11], v[216:223], v[124:127], v243, v243 op_sel_hi:[0,0,0]
	v_mfma_scale_f32_16x16x128_f8f6f4 v[96:99], v[12:19], v[224:231], v[96:99], v243, v243 op_sel_hi:[0,0,0]
	v_mfma_scale_f32_16x16x128_f8f6f4 v[88:91], v[4:11], v[224:231], v[88:91], v243, v243 op_sel_hi:[0,0,0]
	s_setprio 0
	s_barrier
	s_mov_b32 m0, s34
	v_lshl_add_u64 v[182:183], v[182:183], 0, s[24:25]
	ds_read_b128 v[190:193], v186 offset:49152
	ds_read_b128 v[194:197], v186 offset:50176
	ds_read_b128 v[198:201], v186 offset:51200
	ds_read_b128 v[202:205], v186 offset:52224
	ds_read_b128 v[216:219], v186 offset:53248
	ds_read_b128 v[220:223], v186 offset:54272
	ds_read_b128 v[224:227], v186 offset:55296
	ds_read_b128 v[228:231], v186 offset:56320
	global_load_lds_dwordx4 v[182:183], off
	v_lshl_add_u64 v[182:183], v[206:207], 0, s[24:25]
	s_mov_b32 m0, s35
	v_lshl_add_u64 v[176:177], v[176:177], 0, s[88:89]
	global_load_lds_dwordx4 v[182:183], off
	v_readfirstlane_b32 s22, v176
	v_readfirstlane_b32 s23, v177
	s_mov_b32 m0, s46
	v_lshl_add_u64 v[176:177], v[180:181], 0, s[24:25]
	s_nop 2
	global_load_lds_dwordx4 v164, s[22:23]
	s_mov_b32 m0, s47
	s_nop 0
	global_load_lds_dwordx4 v168, s[22:23]
	s_mov_b32 m0, s51
	s_nop 0
	global_load_lds_dwordx4 v[176:177], off
	v_lshl_add_u64 v[176:177], v[178:179], 0, s[24:25]
	s_mov_b32 m0, s52
	s_nop 0
	global_load_lds_dwordx4 v[176:177], off
	s_waitcnt vmcnt(8)
	s_waitcnt lgkmcnt(0)
	s_barrier
	s_setprio 1
	s_waitcnt lgkmcnt(0)
	v_mfma_scale_f32_16x16x128_f8f6f4 v[104:107], v[20:27], v[190:197], v[104:107], v243, v243 op_sel_hi:[0,0,0]
	v_mfma_scale_f32_16x16x128_f8f6f4 v[100:103], v[28:35], v[190:197], v[100:103], v243, v243 op_sel_hi:[0,0,0]
	v_mfma_scale_f32_16x16x128_f8f6f4 v[76:79], v[20:27], v[198:205], v[76:79], v243, v243 op_sel_hi:[0,0,0]
	v_mfma_scale_f32_16x16x128_f8f6f4 v[68:71], v[28:35], v[198:205], v[68:71], v243, v243 op_sel_hi:[0,0,0]
	v_mfma_scale_f32_16x16x128_f8f6f4 v[64:67], v[20:27], v[216:223], v[64:67], v243, v243 op_sel_hi:[0,0,0]
	v_mfma_scale_f32_16x16x128_f8f6f4 v[60:63], v[28:35], v[216:223], v[60:63], v243, v243 op_sel_hi:[0,0,0]
	v_mfma_scale_f32_16x16x128_f8f6f4 v[48:51], v[20:27], v[224:231], v[48:51], v243, v243 op_sel_hi:[0,0,0]
	v_mfma_scale_f32_16x16x128_f8f6f4 v[44:47], v[28:35], v[224:231], v[44:47], v243, v243 op_sel_hi:[0,0,0]
	s_setprio 0
	s_setprio 1
	v_mfma_scale_f32_16x16x128_f8f6f4 v[112:115], v[12:19], v[190:197], v[112:115], v243, v243 op_sel_hi:[0,0,0]
	v_mfma_scale_f32_16x16x128_f8f6f4 v[108:111], v[4:11], v[190:197], v[108:111], v243, v243 op_sel_hi:[0,0,0]
	v_mfma_scale_f32_16x16x128_f8f6f4 v[80:83], v[12:19], v[198:205], v[80:83], v243, v243 op_sel_hi:[0,0,0]
	v_mfma_scale_f32_16x16x128_f8f6f4 v[72:75], v[4:11], v[198:205], v[72:75], v243, v243 op_sel_hi:[0,0,0]
	v_mfma_scale_f32_16x16x128_f8f6f4 v[56:59], v[12:19], v[216:223], v[56:59], v243, v243 op_sel_hi:[0,0,0]
	v_mfma_scale_f32_16x16x128_f8f6f4 v[52:55], v[4:11], v[216:223], v[52:55], v243, v243 op_sel_hi:[0,0,0]
	v_mfma_scale_f32_16x16x128_f8f6f4 v[40:43], v[12:19], v[224:231], v[40:43], v243, v243 op_sel_hi:[0,0,0]
	v_mfma_scale_f32_16x16x128_f8f6f4 v[36:39], v[4:11], v[224:231], v[36:39], v243, v243 op_sel_hi:[0,0,0]
	s_setprio 0
	s_barrier
	s_add_i32 s63, s63, 2
	s_add_u32 s20, s20, 0x100
	s_addc_u32 s21, s21, 0
	s_cmp_gt_u32 s63, 25
	s_cbranch_scc0 .LBB0_1718
	s_nop 15
	s_and_b64 vcc, exec, s[14:15]
	s_cbranch_vccz .LBB0_1721
	s_barrier
